# moe_stagger triangle delays 0,1,2,3,4,3,2,1 x 1.5us (max 6us instead of 10.5us)
# speedup vs baseline: 1.0021x; 1.0016x over previous
.LBB0_1847:
	s_or_b64 exec, exec, s[0:1]
	v_readlane_b32 s0, v254, 4
	s_mov_b32 s2, 0
	s_mov_b32 s4, s0
	v_readlane_b32 s54, v254, 2
	v_readlane_b32 s0, v254, 3
	s_waitcnt lgkmcnt(0)
	s_barrier
	s_lshr_b32 s98, s4, 3
	s_and_b32 s98, s98, 7
	s_sub_u32 s99, 8, s98
	s_min_u32 s98, s98, s99
	s_cmp_eq_u32 s98, 0
	s_cbranch_scc1 .Lstg_done
